# v21 + gate path staging of Wz/Wg: loads batched behind one wait per ds_write group instead of one wait per pair
# baseline (speedup 1.0000x reference)
.LBB0_127:
	v_lshl_add_u64 v[10:11], v[2:3], 0, s[2:3]
	v_add_co_u32_e32 v6, vcc, 0xc000, v10
	s_add_u32 s2, s2, 0x60400
	s_nop 0
	v_addc_co_u32_e32 v7, vcc, 0, v11, vcc
	v_add_co_u32_e32 v8, vcc, 0x6000, v10
	s_addc_u32 s3, s3, 0
	s_nop 0
	v_addc_co_u32_e32 v9, vcc, 0, v11, vcc
	global_load_dword v226, v[6:7], off offset:64
	global_load_dword v227, v[8:9], off
	v_add_co_u32_e32 v8, vcc, 0x18000, v10
	s_cmp_lg_u32 s2, 0x181000
	s_nop 0
	v_addc_co_u32_e32 v9, vcc, 0, v11, vcc
	v_add_co_u32_e32 v12, vcc, 0x12000, v10
	s_nop 0
	v_addc_co_u32_e32 v13, vcc, 0, v11, vcc
	global_load_dword v228, v[8:9], off offset:192
	global_load_dword v229, v[12:13], off offset:128
	v_add_co_u32_e32 v8, vcc, 0x24000, v10
	s_nop 0
	v_addc_co_u32_e32 v9, vcc, 0, v11, vcc
	v_add_co_u32_e32 v12, vcc, 0x1e000, v10
	s_nop 1
	v_addc_co_u32_e32 v13, vcc, 0, v11, vcc
	global_load_dword v230, v[8:9], off offset:320
	s_nop 0
	global_load_dword v231, v[12:13], off offset:256
	v_add_co_u32_e32 v12, vcc, 0x30000, v10
	s_nop 0
	v_addc_co_u32_e32 v13, vcc, 0, v11, vcc
	v_add_co_u32_e32 v14, vcc, 0x2a000, v10
	s_nop 1
	v_addc_co_u32_e32 v15, vcc, 0, v11, vcc
	global_load_dword v232, v[12:13], off offset:448
	global_load_dword v233, v[14:15], off offset:384
	v_add_co_u32_e32 v12, vcc, 0x3c000, v10
	s_nop 0
	v_addc_co_u32_e32 v13, vcc, 0, v11, vcc
	v_add_co_u32_e32 v14, vcc, 0x36000, v10
	s_nop 1
	v_addc_co_u32_e32 v15, vcc, 0, v11, vcc
	global_load_dword v234, v[12:13], off offset:576
	global_load_dword v235, v[14:15], off offset:512
	v_add_co_u32_e32 v12, vcc, 0x48000, v10
	s_waitcnt vmcnt(2)
	v_cvt_pk_bf16_f32 v6, v227, v226
	v_cvt_pk_bf16_f32 v7, v229, v228
	v_cvt_pk_bf16_f32 v8, v231, v230
	v_cvt_pk_bf16_f32 v9, v233, v232
	ds_write_b128 v4, v[6:9]
	s_nop 0
	v_addc_co_u32_e32 v13, vcc, 0, v11, vcc
	v_add_co_u32_e32 v14, vcc, 0x42000, v10
	s_nop 0
	v_addc_co_u32_e32 v15, vcc, 0, v11, vcc
	global_load_dword v237, v[12:13], off offset:704
	global_load_dword v238, v[14:15], off offset:640
	v_add_co_u32_e32 v8, vcc, 0x54000, v10
	s_nop 0
	v_addc_co_u32_e32 v9, vcc, 0, v11, vcc
	v_add_co_u32_e32 v12, vcc, 0x4e000, v10
	s_nop 1
	v_addc_co_u32_e32 v13, vcc, 0, v11, vcc
	global_load_dword v239, v[8:9], off offset:832
	s_nop 0
	global_load_dword v240, v[12:13], off offset:768
	v_add_co_u32_e32 v12, vcc, 0x60000, v10
	s_nop 0
	v_addc_co_u32_e32 v13, vcc, 0, v11, vcc
	v_add_co_u32_e32 v10, vcc, 0x5a000, v10
	s_nop 1
	v_addc_co_u32_e32 v11, vcc, 0, v11, vcc
	global_load_dword v241, v[12:13], off offset:960
	global_load_dword v242, v[10:11], off offset:896
	s_waitcnt vmcnt(0)
	v_cvt_pk_bf16_f32 v6, v235, v234
	v_cvt_pk_bf16_f32 v7, v238, v237
	v_cvt_pk_bf16_f32 v8, v240, v239
	v_cvt_pk_bf16_f32 v9, v242, v241
	ds_write_b128 v4, v[6:9] offset:16
	v_add_u32_e32 v4, 32, v4
	s_cbranch_scc1 .LBB0_127
	v_mov_b32_e32 v2, 0
	v_lshlrev_b32_e32 v12, 2, v0
	v_mov_b32_e32 v13, v2
	v_lshl_add_u64 v[10:11], s[64:65], 0, v[12:13]
	v_add_co_u32_e32 v14, vcc, 0x1000, v10
	s_add_i32 s2, 0, 0x10100
	s_nop 0
	v_addc_co_u32_e32 v15, vcc, 0, v11, vcc
	global_load_dword v243, v[14:15], off
	global_load_dword v245, v12, s[64:65]
	v_add_co_u32_e32 v16, vcc, 0x3000, v10
	v_lshl_add_u32 v44, v0, 5, s2
	s_nop 0
	v_addc_co_u32_e32 v17, vcc, 0, v11, vcc
	v_add_co_u32_e32 v18, vcc, 0x2000, v10
	v_lshlrev_b32_e32 v67, 5, v130
	s_nop 0
	v_addc_co_u32_e32 v19, vcc, 0, v11, vcc
	v_add_co_u32_e32 v20, vcc, 0x5000, v10
	v_and_b32_e32 v66, 48, v0
	s_nop 0
	v_addc_co_u32_e32 v21, vcc, 0, v11, vcc
	v_add_co_u32_e32 v22, vcc, 0x4000, v10
	v_cmp_gt_u32_e64 s[4:5], 32, v236
	s_nop 0
	v_addc_co_u32_e32 v23, vcc, 0, v11, vcc
	v_add_co_u32_e32 v24, vcc, 0x7000, v10
	s_mov_b32 s3, 0
	s_nop 0
	v_addc_co_u32_e32 v25, vcc, 0, v11, vcc
	v_add_co_u32_e32 v26, vcc, 0x6000, v10
	v_add3_u32 v64, s2, v67, v66
	s_nop 0
	v_addc_co_u32_e32 v27, vcc, 0, v11, vcc
	v_add_co_u32_e32 v28, vcc, 0x9000, v10
	global_load_dword v246, v[16:17], off
	global_load_dword v247, v[18:19], off
	v_addc_co_u32_e32 v29, vcc, 0, v11, vcc
	v_add_co_u32_e32 v30, vcc, 0x8000, v10
	global_load_dword v248, v[20:21], off
	global_load_dword v249, v[22:23], off
	v_addc_co_u32_e32 v31, vcc, 0, v11, vcc
	v_add_co_u32_e32 v32, vcc, 0xb000, v10
	global_load_dword v250, v[24:25], off
	global_load_dword v251, v[26:27], off
	v_addc_co_u32_e32 v33, vcc, 0, v11, vcc
	v_add_co_u32_e32 v34, vcc, 0xa000, v10
	global_load_dword v252, v[28:29], off
	global_load_dword v253, v[30:31], off
	v_addc_co_u32_e32 v35, vcc, 0, v11, vcc
	v_add_co_u32_e32 v36, vcc, 0xd000, v10
	global_load_dword v226, v[32:33], off
	global_load_dword v227, v[34:35], off
	v_addc_co_u32_e32 v37, vcc, 0, v11, vcc
	v_add_co_u32_e32 v38, vcc, 0xc000, v10
	s_nop 0
	v_addc_co_u32_e32 v39, vcc, 0, v11, vcc
	global_load_dword v228, v[36:37], off
	global_load_dword v229, v[38:39], off
	v_add_co_u32_e32 v40, vcc, 0xf000, v10
	s_nop 1
	v_addc_co_u32_e32 v41, vcc, 0, v11, vcc
	v_add_co_u32_e32 v42, vcc, 0xe000, v10
	s_nop 0
	v_addc_co_u32_e32 v43, vcc, 0, v11, vcc
	global_load_dword v230, v[40:41], off
	global_load_dword v231, v[42:43], off
	global_load_dword v232, v[14:15], off offset:2048
	global_load_dword v233, v12, s[64:65] offset:2048
	s_waitcnt vmcnt(2)
	v_cvt_pk_bf16_f32 v4, v245, v243
	v_cvt_pk_bf16_f32 v5, v247, v246
	v_cvt_pk_bf16_f32 v6, v249, v248
	v_cvt_pk_bf16_f32 v7, v251, v250
	v_cvt_pk_bf16_f32 v8, v253, v252
	v_cvt_pk_bf16_f32 v9, v227, v226
	v_cvt_pk_bf16_f32 v10, v229, v228
	v_cvt_pk_bf16_f32 v11, v231, v230
	ds_write_b128 v44, v[4:7]
	ds_write_b128 v44, v[8:11] offset:16
	v_mov_b32_e32 v6, 0
	v_mov_b32_e32 v7, 0
	v_mov_b32_e32 v8, 0
	v_mov_b32_e32 v9, 0
	global_load_dword v234, v[16:17], off offset:2048
	global_load_dword v235, v[18:19], off offset:2048
	global_load_dword v237, v[20:21], off offset:2048
	global_load_dword v238, v[22:23], off offset:2048
	global_load_dword v239, v[24:25], off offset:2048
	global_load_dword v240, v[26:27], off offset:2048
	global_load_dword v241, v[28:29], off offset:2048
	global_load_dword v242, v[30:31], off offset:2048
	global_load_dword v243, v[32:33], off offset:2048
	global_load_dword v245, v[34:35], off offset:2048
	global_load_dword v246, v[36:37], off offset:2048
	global_load_dword v247, v[38:39], off offset:2048
	global_load_dword v248, v[40:41], off offset:2048
	global_load_dword v249, v[42:43], off offset:2048
	s_waitcnt vmcnt(0)
	v_cvt_pk_bf16_f32 v10, v233, v232
	v_cvt_pk_bf16_f32 v11, v235, v234
	v_cvt_pk_bf16_f32 v12, v238, v237
	v_cvt_pk_bf16_f32 v13, v240, v239
	v_cvt_pk_bf16_f32 v14, v242, v241
	v_cvt_pk_bf16_f32 v15, v245, v243
	v_cvt_pk_bf16_f32 v16, v247, v246
	v_cvt_pk_bf16_f32 v17, v249, v248
	ds_write_b128 v44, v[10:13] offset:16384
	ds_write_b128 v44, v[14:17] offset:16400
	s_waitcnt lgkmcnt(0)
	s_barrier
	s_and_saveexec_b64 s[6:7], s[4:5]
	v_lshl_add_u32 v3, s95, 12, v64
	ds_read_b128 v[6:9], v3
	s_or_b64 exec, exec, s[6:7]
	v_and_b32_e32 v4, 48, v236
	v_mov_b32_e32 v5, v2
	v_lshl_add_u64 v[62:63], s[66:67], 0, v[4:5]
	s_lshl_b32 s2, s95, 7
	v_lshl_add_u64 v[4:5], s[2:3], 2, v[62:63]
	global_load_dwordx4 v[10:13], v[4:5], off
	s_lshl_b32 s10, s95, 3
	s_or_b32 s8, s10, 1
	v_mov_b32_e32 v3, 0
	v_mov_b32_e32 v4, 0
	v_mov_b32_e32 v5, 0
	s_and_saveexec_b64 s[6:7], s[4:5]
	v_lshl_add_u32 v2, s8, 9, v64
	ds_read_b128 v[2:5], v2
	s_or_b64 exec, exec, s[6:7]
	s_lshl_b32 s6, s8, 4
	s_mov_b32 s7, s3
	v_lshl_add_u64 v[14:15], s[6:7], 2, v[62:63]
	global_load_dwordx4 v[14:17], v[14:15], off
	s_or_b32 s6, s10, 2
	s_mov_b32 s7, 0
	v_mov_b32_e32 v18, 0
	v_mov_b32_e32 v22, 0
	v_mov_b32_e32 v23, 0
	v_mov_b32_e32 v24, 0
	v_mov_b32_e32 v25, 0
	s_and_saveexec_b64 s[8:9], s[4:5]
	v_lshl_add_u32 v19, s6, 9, v64
	ds_read_b128 v[22:25], v19
	s_or_b64 exec, exec, s[8:9]
	s_lshl_b32 s6, s6, 4
	v_lshl_add_u64 v[20:21], s[6:7], 2, v[62:63]
	global_load_dwordx4 v[26:29], v[20:21], off
	s_or_b32 s6, s10, 3
	v_mov_b32_e32 v19, 0
	v_mov_b32_e32 v20, 0
	v_mov_b32_e32 v21, 0
	s_and_saveexec_b64 s[8:9], s[4:5]
	v_lshl_add_u32 v18, s6, 9, v64
	ds_read_b128 v[18:21], v18
	s_or_b64 exec, exec, s[8:9]
	s_lshl_b32 s6, s6, 4
	v_lshl_add_u64 v[30:31], s[6:7], 2, v[62:63]
	global_load_dwordx4 v[30:33], v[30:31], off
	s_or_b32 s6, s10, 4
	v_mov_b32_e32 v34, 0
	v_mov_b32_e32 v38, 0
	v_mov_b32_e32 v39, 0
	v_mov_b32_e32 v40, 0
	v_mov_b32_e32 v41, 0
	s_and_saveexec_b64 s[8:9], s[4:5]
	v_lshl_add_u32 v35, s6, 9, v64
	ds_read_b128 v[38:41], v35
	s_or_b64 exec, exec, s[8:9]
	s_lshl_b32 s6, s6, 4
	v_lshl_add_u64 v[36:37], s[6:7], 2, v[62:63]
	global_load_dwordx4 v[42:45], v[36:37], off
	s_or_b32 s6, s10, 5
	v_mov_b32_e32 v35, 0
	v_mov_b32_e32 v36, 0
	v_mov_b32_e32 v37, 0
	s_and_saveexec_b64 s[8:9], s[4:5]
	v_lshl_add_u32 v34, s6, 9, v64
	ds_read_b128 v[34:37], v34
	s_or_b64 exec, exec, s[8:9]
	s_lshl_b32 s6, s6, 4
	v_lshl_add_u64 v[46:47], s[6:7], 2, v[62:63]
	global_load_dwordx4 v[46:49], v[46:47], off
	s_or_b32 s6, s10, 6
	v_mov_b32_e32 v50, 0
	v_mov_b32_e32 v54, 0
	v_mov_b32_e32 v55, 0
	v_mov_b32_e32 v56, 0
	v_mov_b32_e32 v57, 0
	s_and_saveexec_b64 s[8:9], s[4:5]
	v_lshl_add_u32 v51, s6, 9, v64
	ds_read_b128 v[54:57], v51
	s_or_b64 exec, exec, s[8:9]
	s_lshl_b32 s6, s6, 4
	v_lshl_add_u64 v[52:53], s[6:7], 2, v[62:63]
	global_load_dwordx4 v[58:61], v[52:53], off
	s_or_b32 s8, s10, 7
	v_mov_b32_e32 v51, 0
	v_mov_b32_e32 v52, 0
	v_mov_b32_e32 v53, 0
	s_and_saveexec_b64 s[6:7], s[4:5]
	v_lshl_add_u32 v50, s8, 9, v64
	ds_read_b128 v[50:53], v50
	s_or_b64 exec, exec, s[6:7]
	v_readlane_b32 s6, v254, 0
	s_cmpk_lt_i32 s6, 0x100
	v_readlane_b32 s7, v254, 1
	s_cbranch_scc0 .LBB0_161
	s_lshl_b32 s24, s8, 4
	s_mov_b32 s25, 0
	v_lshl_add_u64 v[62:63], s[24:25], 2, v[62:63]
	global_load_dwordx4 v[62:65], v[62:63], off
	v_readlane_b32 s9, v254, 2
	s_lshr_b32 s6, s9, 8
	s_bfe_u32 s8, s9, 0x20006
	s_lshl_b32 s7, s6, 11
	v_lshrrev_b32_e32 v68, 4, v236
	s_lshl_b32 s28, s8, 4
	s_lshl_b32 s24, s6, 10
	s_add_i32 s7, s7, 0
	v_lshlrev_b32_e32 v70, 4, v68
	s_cmp_eq_u32 s6, 1
	v_add3_u32 v1, s7, v1, v70
	s_cselect_b64 s[6:7], -1, 0
	s_lshl_b32 s8, s8, 10
	s_add_i32 s31, 0, 0x18100
	s_add_i32 s29, s31, s8
	v_lshlrev_b32_e32 v69, 2, v68
	s_cmpk_lt_u32 s9, 0x100
	s_cselect_b64 s[8:9], -1, 0
	s_lshl_b32 s10, s95, 10
	v_lshlrev_b32_e32 v72, 2, v69
	v_mov_b32_e32 v73, 0
	v_readlane_b32 s26, v254, 0
	s_add_i32 s31, s31, s10
	s_add_i32 s12, 0, 0x19100
	v_or_b32_e32 v76, s28, v69
	v_lshl_add_u64 v[68:69], s[58:59], 0, v[72:73]
	s_mov_b64 s[10:11], 0x41680000
	v_readlane_b32 s27, v254, 1
	s_mov_b32 s72, s26
	s_ashr_i32 s73, s26, 31
	v_lshl_add_u32 v71, v130, 1, s12
	v_lshl_add_u64 v[74:75], v[68:69], 0, s[10:11]
	v_add3_u32 v72, s12, v67, v70
	s_or_b32 s10, s2, 16
	s_mov_b32 s11, s25
	s_or_b32 s12, s2, 32
	s_mov_b32 s13, s25
	s_or_b32 s14, s2, 48
	s_mov_b32 s15, s25
	s_or_b32 s16, s2, 64
	s_mov_b32 s17, s25
	s_or_b32 s18, s2, 0x50
	s_mov_b32 s19, s25
	s_or_b32 s20, s2, 0x60
	s_mov_b32 s21, s25
	s_or_b32 s22, s2, 0x70
	s_mov_b32 s23, s25
	s_lshl_b64 s[26:27], s[72:73], 18
	v_or_b32_e32 v67, s28, v130
	s_lshl_b64 s[24:25], s[24:25], 1
	v_lshlrev_b32_e32 v67, 12, v67
	s_add_u32 s24, s58, s24
	v_or3_b32 v66, s26, v67, v66
	v_mov_b32_e32 v67, s27
	s_addc_u32 s25, s59, s25
	s_mov_b32 s70, s72
	v_lshlrev_b32_e32 v68, 5, v76
	v_lshl_add_u64 v[66:67], s[24:25], 0, v[66:67]
	s_mov_b64 s[24:25], 0x31680100
	s_ashr_i32 s97, s96, 31
	v_writelane_b32 v254, s70, 0
	v_lshlrev_b32_e32 v84, 4, v236
	v_lshl_add_u64 v[76:77], v[66:67], 0, s[24:25]
	s_lshl_b64 s[24:25], s[96:97], 18
	s_mov_b64 s[26:27], 0x200
	v_add_u32_e32 v85, v71, v68
	s_mov_b32 s35, 0xbfb8aa3b
	s_mov_b32 s37, 0x3f2aaaab
	s_mov_b32 s28, 0x3f317218
	s_mov_b32 s30, 0xb102e308
	s_mov_b32 s34, 0x3ecc95a3
	s_mov_b32 s36, 0x3e9b6dac
	s_mov_b32 s42, 0x3f2aaada
	s_mov_b32 s43, 0x7f800000
	s_mov_b32 s45, 0x33800000
	s_mov_b32 s44, 0x3d800000
	s_mov_b64 s[62:63], 0x10000
	s_mov_b64 s[64:65], 0x20000
	s_mov_b64 s[66:67], 0x30000
	v_mov_b32_e32 v86, 0x7f800000
	v_mov_b32_e32 v87, 0x7fc00000
	v_mov_b32_e32 v88, 0xff800000
	v_writelane_b32 v254, s71, 1
	s_mov_b32 s70, s72
	s_branch .LBB0_147
